# row-step table read hoist also in the two L3 GU epilogues (spare VGPRs v222-227)
# speedup vs baseline: 1.0037x; 1.0001x over previous
; __device__ __forceinline__ float fast_sigmoid(float x) { return __builtin_amdgcn_rcpf(1.0f + __expf(-x)); }
;     __device__ __forceinline__ void operator()(const f32x4 (&acc)[2][2][4][2], const Unit& u, int wr, int wc, int fr, int fq) const {
;         const int row0 = u.pm * BM + wr * 64 + fr, col0 = u.pn * HALF + wc * 32 + 8 * fq; const int sl = IN8 ? rt.slot(u.pm) : 0;
;         f32x4 cg[2], cu[2];
; #pragma unroll
;         for (int n = 0; n < 2; ++n) { cg[n] = IN8 ? *(const f32x4*)(cstep + u.pn * BM + wc * 32 + 8 * fq + 4 * n) : (f32x4){1.f, 1.f, 1.f, 1.f}; cu[n] = IN8 ? *(const f32x4*)(cstep + u.pn * BM + HALF + wc * 32 + 8 * fq + 4 * n) : (f32x4){1.f, 1.f, 1.f, 1.f}; }
; #pragma unroll
;         for (int ai = 0; ai < 2; ++ai)
; #pragma unroll
;             for (int m = 0; m < 4; ++m) { const size_t off = (size_t)(row0 + ai * HALF + m * 16) * ldc + col0;
;                 const float rs = IN8 ? rt.tab[sl * 256 + wr * 64 + ai * HALF + m * 16 + fr] : isc;
;                 const float rsn = rs * -1.4426950408889634f, rs2 = rs * rs; (void)rsn; (void)rs2;
;                 float o[8];
; #pragma unroll
;                 for (int n = 0; n < 2; ++n)
; #pragma unroll
;                     for (int e = 0; e < 4; ++e) { const float ga = acc[ai][0][m][n][e], ua = acc[ai][1][m][n][e];
;                         if (IN8) {
;                             const float gq = (float)__float_as_int(ga) * cg[n][e], uq = (float)__float_as_int(ua) * cu[n][e];
;                             const float sg = __builtin_amdgcn_rcpf(1.0f + __builtin_amdgcn_exp2f(gq * rsn));
;                             o[4 * n + e] = (gq * uq) * (sg * rs2); }
;                         else { const float g = ga * rs, up = ua * rs; o[4 * n + e] = g * fast_sigmoid(g) * up; } }
;                 if (F8) { unsigned w0 = 0u, w1 = 0u;
; #pragma unroll
;                     for (int e = 0; e < 8; ++e) o[e] = __builtin_amdgcn_fmed3f(o[e] * H8_SCALE, -448.0f, 448.0f);
;                     w0 = __builtin_amdgcn_cvt_pk_fp8_f32(o[0], o[1], w0, false); w0 = __builtin_amdgcn_cvt_pk_fp8_f32(o[2], o[3], w0, true);
;                     w1 = __builtin_amdgcn_cvt_pk_fp8_f32(o[4], o[5], w1, false); w1 = __builtin_amdgcn_cvt_pk_fp8_f32(o[6], o[7], w1, true);
;                     typedef unsigned u32x2_ __attribute__((ext_vector_type(2))); *(u32x2_*)((unsigned char*)O + off) = (u32x2_){w0, w1}; }
.LBB0_4144:
	s_lshl_b32 s24, s64, 8
	s_ashr_i32 s25, s24, 31
	v_lshl_add_u64 v[122:123], s[24:25], 2, v[150:151]
	global_load_dwordx4 v[170:173], v[122:123], off
	global_load_dwordx4 v[130:133], v[122:123], off offset:512
	global_load_dwordx4 v[126:129], v[122:123], off offset:16
	s_nop 0
	global_load_dwordx4 v[122:125], v[122:123], off offset:528
	s_add_i32 s15, s34, 0x20204
	v_cvt_f32_i32_e32 v182, v114
	v_mov_b32_e32 v114, s15
	v_cvt_f32_i32_e32 v174, v134
	v_cvt_f32_i32_e32 v176, v135
	ds_read2_b32 v[134:135], v114 offset1:1
	s_add_i32 s17, s34, 0x2020c
	s_add_i32 s24, s34, 0x20214
	s_add_i32 s25, s34, 0x2021c
	v_cvt_f32_i32_e32 v175, v138
	v_cvt_f32_i32_e32 v183, v118
	v_mov_b32_e32 v118, s17
	v_mov_b32_e32 v138, s24
	v_mov_b32_e32 v114, s25
	v_cvt_f32_i32_e32 v177, v139
	v_cvt_f32_i32_e32 v178, v136
	v_cvt_f32_i32_e32 v180, v137
	ds_read2_b32 v[136:137], v118 offset1:1
	ds_read2_b32 v[138:139], v138 offset1:1
	ds_read_b32 v114, v114
	s_waitcnt lgkmcnt(0)
	v_cmp_eq_u32_e32 vcc, s22, v134
	v_cvt_f32_i32_e32 v179, v140
	v_cvt_f32_i32_e32 v181, v141
	v_cndmask_b32_e64 v118, 0, 1, vcc
	v_cmp_ne_u32_e32 vcc, s22, v135
	v_cvt_f32_i32_e32 v119, v119
	v_cvt_f32_i32_e32 v160, v116
	v_cndmask_b32_e32 v118, 2, v118, vcc
	v_cmp_ne_u32_e32 vcc, s22, v136
	v_cvt_f32_i32_e32 v121, v121
	v_cvt_f32_i32_e32 v111, v111
	v_cndmask_b32_e32 v118, 3, v118, vcc
	v_cmp_ne_u32_e32 vcc, s22, v137
	v_cvt_f32_i32_e32 v103, v103
	v_lshl_or_b32 v162, s64, 7, v165
	v_cndmask_b32_e32 v118, 4, v118, vcc
	v_cmp_ne_u32_e32 vcc, s22, v138
	v_lshl_add_u32 v169, s22, 8, v1
	v_ashrrev_i32_e32 v163, 31, v162
	v_cndmask_b32_e32 v118, 5, v118, vcc
	v_cmp_ne_u32_e32 vcc, s22, v139
	v_cvt_f32_i32_e32 v113, v113
	v_cvt_f32_i32_e32 v105, v105
	v_cndmask_b32_e32 v118, 6, v118, vcc
	v_cmp_ne_u32_e32 vcc, s22, v114
	v_cvt_f32_i32_e32 v95, v95
	v_cvt_f32_i32_e32 v87, v87
	v_cndmask_b32_e32 v114, 7, v118, vcc
	v_cvt_f32_i32_e32 v118, v115
	v_readfirstlane_b32 s15, v114
	v_cvt_f32_i32_e32 v97, v97
	v_cvt_f32_i32_e32 v89, v89
	v_lshl_add_u32 v140, s15, 10, v166
	ds_read2_b32 v[138:139], v140 offset1:16
	ds_read2_b32 v[222:223], v140 offset0:32 offset1:48
	ds_read2_b32 v[224:225], v140 offset0:128 offset1:144
	ds_read2_b32 v[226:227], v140 offset0:160 offset1:176
	v_cvt_f32_i32_e32 v79, v79
	v_cvt_f32_i32_e32 v71, v71
	v_cvt_f32_i32_e32 v81, v81
	v_cvt_f32_i32_e32 v73, v73
	s_waitcnt lgkmcnt(0)
	v_mov_b32_e32 v185, v138
	v_cvt_f32_i32_e32 v63, v63
	v_cvt_f32_i32_e32 v55, v55
	v_cvt_f32_i32_e32 v65, v65
	v_cvt_f32_i32_e32 v57, v57
	v_cvt_f32_i32_e32 v47, v47
	v_cvt_f32_i32_e32 v39, v39
	v_cvt_f32_i32_e32 v49, v49
	v_cvt_f32_i32_e32 v41, v41
	v_cvt_f32_i32_e32 v31, v31
	v_cvt_f32_i32_e32 v23, v23
	v_cvt_f32_i32_e32 v33, v33
	v_cvt_f32_i32_e32 v25, v25
	v_cvt_f32_i32_e32 v15, v15
	v_cvt_f32_i32_e32 v7, v7
	v_cvt_f32_i32_e32 v17, v17
	v_cvt_f32_i32_e32 v9, v9
	s_andn2_b64 vcc, exec, s[0:1]
	s_mov_b64 s[0:1], -1
	s_waitcnt vmcnt(0)
	v_mov_b32_e32 v136, v170
	v_mov_b32_e32 v137, v130
	v_mov_b32_e32 v130, v171
	v_mov_b32_e32 v134, v172
	v_mov_b32_e32 v135, v132
	v_mov_b32_e32 v132, v173
	v_mov_b32_e32 v114, v126
	v_mov_b32_e32 v115, v122
	v_mov_b32_e32 v122, v127
	v_mov_b32_e32 v184, v128
	v_pk_mul_f32 v[126:127], v[136:137], v[174:175]
	v_pk_mul_f32 v[170:171], v[130:131], v[176:177]
	v_pk_mul_f32 v[172:173], v[134:135], v[178:179]
	v_pk_mul_f32 v[174:175], v[132:133], v[180:181]
	v_pk_mul_f32 v[176:177], v[114:115], v[182:183]
	v_pk_mul_f32 v[118:119], v[122:123], v[118:119]
	v_pk_mul_f32 v[178:179], v[184:185], v[160:161]
	v_mul_f32_e32 v160, v172, v173
	v_mul_f32_e32 v173, v174, v175
	v_mul_f32_e32 v175, v176, v177
	v_mul_f32_e32 v177, v118, v119
	v_mul_f32_e32 v119, v126, v179
	v_mul_f32_e32 v116, v126, v127
	v_mul_f32_e32 v141, v170, v171
	v_mul_f32_e32 v126, v170, v179
	v_mul_f32_e32 v170, v174, v179
	v_exp_f32_e32 v119, v119
	v_mul_f32_e32 v171, v176, v179
	v_exp_f32_e32 v170, v170
	v_exp_f32_e32 v171, v171
	v_add_f32_e32 v119, 1.0, v119
	v_mul_f32_e32 v118, v118, v179
	v_mul_f32_e32 v127, v172, v179
	v_rcp_f32_e32 v172, v119
	v_add_f32_e32 v119, 1.0, v170
	v_exp_f32_e32 v118, v118
	v_rcp_f32_e32 v176, v119
	v_add_f32_e32 v119, 1.0, v171
	v_exp_f32_e32 v126, v126
	v_rcp_f32_e32 v180, v119
	v_mul_f32_e32 v119, v178, v179
	v_exp_f32_e32 v127, v127
	v_exp_f32_e32 v119, v119
	v_add_f32_e32 v118, 1.0, v118
	v_rcp_f32_e32 v181, v118
	v_cvt_f32_i32_e32 v118, v120
	v_add_f32_e32 v126, 1.0, v126
	v_add_f32_e32 v127, 1.0, v127
	v_rcp_f32_e32 v126, v126
	v_add_f32_e32 v119, 1.0, v119
	v_rcp_f32_e32 v174, v127
	v_rcp_f32_e32 v127, v119
	v_mov_b32_e32 v170, v124
	v_mov_b32_e32 v171, v138
	v_mov_b32_e32 v119, v138
	v_pk_mul_f32 v[118:119], v[170:171], v[118:119]
	s_nop 0
	v_mul_f32_e32 v120, v119, v172
	v_mul_f32_e32 v138, v116, v120
	v_mul_f32_e32 v116, v119, v126
	v_mul_f32_e32 v141, v141, v116
	v_mul_f32_e32 v116, v119, v174
	v_cvt_f32_i32_e32 v120, v117
	v_mul_f32_e32 v160, v160, v116
	v_mul_f32_e32 v116, v119, v176
	v_mul_f32_e32 v170, v173, v116
	v_mul_f32_e32 v116, v119, v180
	v_mul_f32_e32 v171, v175, v116
	v_mov_b32_e32 v116, v129
	v_mov_b32_e32 v117, v125
	v_pk_mul_f32 v[120:121], v[116:117], v[120:121]
	v_mul_f32_e32 v126, v119, v181
	v_mul_f32_e32 v125, v120, v179
	v_exp_f32_e32 v125, v125
	v_mul_f32_e32 v129, v177, v126
	v_mov_b32_e32 v126, v178
	v_pk_mul_f32 v[126:127], v[118:119], v[126:127]
	v_add_f32_e32 v125, 1.0, v125
	v_rcp_f32_e32 v125, v125
	v_mul_f32_e32 v120, v120, v121
	v_mul_f32_e32 v118, v126, v127
	v_mul_f32_e32 v118, 4.0, v118
	v_mul_f32_e32 v119, v119, v125
	v_mul_f32_e32 v119, v120, v119
	v_mul_f32_e32 v120, 4.0, v138
	v_med3_f32 v121, v120, s62, v168
; __device__ __forceinline__ float fast_sigmoid(float x) { return __builtin_amdgcn_rcpf(1.0f + __expf(-x)); }
;     __device__ __forceinline__ void operator()(const f32x4 (&acc)[2][2][4][2], const Unit& u, int wr, int wc, int fr, int fq) const {
;     ...
;             for (int m = 0; m < 4; ++m) { const size_t off = (size_t)(row0 + ai * HALF + m * 16) * ldc + col0;
;                 const float rs = IN8 ? rt.tab[sl * 256 + wr * 64 + ai * HALF + m * 16 + fr] : isc;
;                 const float rsn = rs * -1.4426950408889634f, rs2 = rs * rs; (void)rsn; (void)rs2;
;                 float o[8];
; #pragma unroll
;                 for (int n = 0; n < 2; ++n)
; #pragma unroll
;                     for (int e = 0; e < 4; ++e) { const float ga = acc[ai][0][m][n][e], ua = acc[ai][1][m][n][e];
;                         if (IN8) {
;                             const float gq = (float)__float_as_int(ga) * cg[n][e], uq = (float)__float_as_int(ua) * cu[n][e];
;                             const float sg = __builtin_amdgcn_rcpf(1.0f + __builtin_amdgcn_exp2f(gq * rsn));
;                             o[4 * n + e] = (gq * uq) * (sg * rs2); }
;                         else { const float g = ga * rs, up = ua * rs; o[4 * n + e] = g * fast_sigmoid(g) * up; } }
;                 if (F8) { unsigned w0 = 0u, w1 = 0u;
; #pragma unroll
;                     for (int e = 0; e < 8; ++e) o[e] = __builtin_amdgcn_fmed3f(o[e] * H8_SCALE, -448.0f, 448.0f);
;                     w0 = __builtin_amdgcn_cvt_pk_fp8_f32(o[0], o[1], w0, false); w0 = __builtin_amdgcn_cvt_pk_fp8_f32(o[2], o[3], w0, true);
;                     w1 = __builtin_amdgcn_cvt_pk_fp8_f32(o[4], o[5], w1, false); w1 = __builtin_amdgcn_cvt_pk_fp8_f32(o[6], o[7], w1, true);
;                     typedef unsigned u32x2_ __attribute__((ext_vector_type(2))); *(u32x2_*)((unsigned char*)O + off) = (u32x2_){w0, w1}; }
	v_mul_f32_e32 v120, 4.0, v141
	v_med3_f32 v125, v120, s62, v168
	v_mul_f32_e32 v120, 4.0, v160
	v_med3_f32 v126, v120, s62, v168
	v_mul_f32_e32 v120, 4.0, v170
	v_med3_f32 v127, v120, s62, v168
	v_mul_f32_e32 v120, 4.0, v171
	v_med3_f32 v138, v120, s62, v168
	v_mul_f32_e32 v120, 4.0, v129
	v_med3_f32 v129, v120, s62, v168
	v_mov_b32_e32 v120, 0
	v_cvt_pk_fp8_f32 v120, v121, v125
	v_mov_b32_e32 v121, 0
	v_cvt_pk_fp8_f32 v121, v138, v129
	v_mul_f32_e32 v119, 4.0, v119
	v_med3_f32 v118, v118, s62, v168
	v_med3_f32 v119, v119, s62, v168
	v_cvt_pk_fp8_f32 v120, v126, v127 op_sel:[0,0,1]
	v_cvt_pk_fp8_f32 v121, v118, v119 op_sel:[0,0,1]
	v_cvt_f32_i32_e32 v171, v110
	v_cvt_f32_i32_e32 v170, v106
	v_cvt_f32_i32_e32 v110, v107
	v_cvt_f32_i32_e32 v107, v112
	v_cvt_f32_i32_e32 v112, v109
	v_cvt_f32_i32_e32 v109, v102
	v_cvt_f32_i32_e32 v160, v100
	v_cvt_f32_i32_e32 v102, v99
	v_mov_b64_e32 v[118:119], s[6:7]
	v_cvt_f32_i32_e32 v106, v108
	v_mad_i64_i32 v[126:127], s[24:25], v169, s63, v[118:119]
	v_lshl_add_u64 v[126:127], v[126:127], 0, v[162:163]
	v_mov_b32_e32 v129, v139
	global_store_dwordx2 v[126:127], v[120:121], off
	v_pk_mul_f32 v[120:121], v[136:137], v[170:171]
	v_pk_mul_f32 v[110:111], v[130:131], v[110:111]
	v_cvt_f32_i32_e32 v108, v98
	v_pk_mul_f32 v[98:99], v[128:129], v[160:161]
	v_pk_mul_f32 v[102:103], v[122:123], v[102:103]
	v_mul_f32_e32 v121, v120, v121
	v_pk_mul_f32 v[106:107], v[134:135], v[106:107]
	v_mul_f32_e32 v100, v120, v99
	v_mul_f32_e32 v120, v102, v103
	v_mul_f32_e32 v103, v110, v99
	v_mul_f32_e32 v127, v106, v107
	v_exp_f32_e32 v103, v103
	v_mul_f32_e32 v106, v106, v99
	v_exp_f32_e32 v106, v106
	v_exp_f32_e32 v100, v100
	v_pk_mul_f32 v[112:113], v[132:133], v[112:113]
	v_add_f32_e32 v103, 1.0, v103
	v_mul_f32_e32 v111, v110, v111
	v_pk_mul_f32 v[108:109], v[114:115], v[108:109]
	v_rcp_f32_e32 v110, v103
	v_add_f32_e32 v103, 1.0, v106
	v_mul_f32_e32 v106, v112, v99
	v_exp_f32_e32 v106, v106
	v_mul_f32_e32 v107, v108, v99
	v_add_f32_e32 v100, 1.0, v100
	v_exp_f32_e32 v107, v107
	v_cvt_f32_i32_e32 v138, v104
	v_rcp_f32_e32 v100, v100
	v_mul_f32_e32 v109, v108, v109
	v_rcp_f32_e32 v108, v103
	v_add_f32_e32 v103, 1.0, v106
	v_mov_b32_e32 v125, v139
	v_mul_f32_e32 v113, v112, v113
	v_rcp_f32_e32 v112, v103
	v_add_f32_e32 v103, 1.0, v107
	v_pk_mul_f32 v[106:107], v[124:125], v[138:139]
	v_mul_f32_e32 v102, v102, v99
	v_rcp_f32_e32 v129, v103
	v_mul_f32_e32 v100, v107, v100
	v_exp_f32_e32 v102, v102
	v_mul_f32_e32 v121, v121, v100
	v_mul_f32_e32 v100, v107, v110
	v_cvt_f32_i32_e32 v104, v101
	v_mul_f32_e32 v110, v111, v100
	v_mul_f32_e32 v100, v107, v108
	v_mul_f32_e32 v108, v127, v100
	v_mul_f32_e32 v100, v107, v112
	v_mul_f32_e32 v111, v113, v100
	v_mul_f32_e32 v100, v107, v129
	v_mul_f32_e32 v103, v98, v99
	v_add_f32_e32 v102, 1.0, v102
	v_mul_f32_e32 v109, v109, v100
	v_pk_mul_f32 v[100:101], v[116:117], v[104:105]
	v_exp_f32_e32 v103, v103
	v_rcp_f32_e32 v102, v102
	v_mul_f32_e32 v99, v100, v99
	v_exp_f32_e32 v99, v99
	v_add_f32_e32 v103, 1.0, v103
	v_mul_f32_e32 v102, v107, v102
	v_rcp_f32_e32 v103, v103
	v_mul_f32_e32 v104, v120, v102
	v_mov_b32_e32 v102, v98
	v_add_f32_e32 v98, 1.0, v99
	v_rcp_f32_e32 v105, v98
	v_pk_mul_f32 v[98:99], v[106:107], v[102:103]
	v_mul_f32_e32 v104, 4.0, v104
	v_mul_f32_e32 v98, v98, v99
	v_mul_f32_e32 v99, v100, v101
	v_mul_f32_e32 v100, v107, v105
	v_mul_f32_e32 v100, v99, v100
	v_mul_f32_e32 v99, 4.0, v121
	v_mul_f32_e32 v101, 4.0, v110
	v_mul_f32_e32 v98, 4.0, v98
	v_med3_f32 v99, v99, s62, v168
	v_med3_f32 v101, v101, s62, v168
	v_mul_f32_e32 v105, 4.0, v109
	v_med3_f32 v106, v98, s62, v168
	v_mov_b32_e32 v98, 0
	v_med3_f32 v105, v105, s62, v168
	v_med3_f32 v104, v104, s62, v168
	v_cvt_pk_fp8_f32 v98, v99, v101
	v_mov_b32_e32 v99, 0
	v_cvt_pk_fp8_f32 v99, v105, v104
	v_mul_f32_e32 v102, 4.0, v108
	v_mul_f32_e32 v103, 4.0, v111
	v_mul_f32_e32 v100, 4.0, v100
	v_med3_f32 v102, v102, s62, v168
	v_med3_f32 v103, v103, s62, v168
	v_med3_f32 v100, v100, s62, v168
	v_cvt_pk_fp8_f32 v98, v102, v103 op_sel:[0,0,1]
	v_cvt_pk_fp8_f32 v99, v106, v100 op_sel:[0,0,1]
	v_or_b32_e32 v126, 16, v169
	v_mad_i64_i32 v[100:101], s[24:25], v126, s63, v[118:119]
	v_lshl_add_u64 v[100:101], v[100:101], 0, v[162:163]
	global_store_dwordx2 v[100:101], v[98:99], off
	s_nop 0
	v_cvt_f32_i32_e32 v103, v94
	v_cvt_f32_i32_e32 v102, v90
	v_cvt_f32_i32_e32 v94, v91
	v_cvt_f32_i32_e32 v91, v96
	v_cvt_f32_i32_e32 v96, v93
	v_cvt_f32_i32_e32 v93, v86
	v_cvt_f32_i32_e32 v160, v84
	v_cvt_f32_i32_e32 v86, v83
	v_cvt_f32_i32_e32 v90, v92
	s_waitcnt lgkmcnt(0)
; __device__ __forceinline__ float fast_sigmoid(float x) { return __builtin_amdgcn_rcpf(1.0f + __expf(-x)); }
;     __device__ __forceinline__ void operator()(const f32x4 (&acc)[2][2][4][2], const Unit& u, int wr, int wc, int fr, int fq) const {
;     ...
;             for (int m = 0; m < 4; ++m) { const size_t off = (size_t)(row0 + ai * HALF + m * 16) * ldc + col0;
;                 const float rs = IN8 ? rt.tab[sl * 256 + wr * 64 + ai * HALF + m * 16 + fr] : isc;
;                 const float rsn = rs * -1.4426950408889634f, rs2 = rs * rs; (void)rsn; (void)rs2;
;                 float o[8];
; #pragma unroll
;                 for (int n = 0; n < 2; ++n)
; #pragma unroll
;                     for (int e = 0; e < 4; ++e) { const float ga = acc[ai][0][m][n][e], ua = acc[ai][1][m][n][e];
;                         if (IN8) {
;                             const float gq = (float)__float_as_int(ga) * cg[n][e], uq = (float)__float_as_int(ua) * cu[n][e];
;                             const float sg = __builtin_amdgcn_rcpf(1.0f + __builtin_amdgcn_exp2f(gq * rsn));
;                             o[4 * n + e] = (gq * uq) * (sg * rs2); }
;                         else { const float g = ga * rs, up = ua * rs; o[4 * n + e] = g * fast_sigmoid(g) * up; } }
;                 if (F8) { unsigned w0 = 0u, w1 = 0u;
; #pragma unroll
;                     for (int e = 0; e < 8; ++e) o[e] = __builtin_amdgcn_fmed3f(o[e] * H8_SCALE, -448.0f, 448.0f);
;                     w0 = __builtin_amdgcn_cvt_pk_fp8_f32(o[0], o[1], w0, false); w0 = __builtin_amdgcn_cvt_pk_fp8_f32(o[2], o[3], w0, true);
;                     w1 = __builtin_amdgcn_cvt_pk_fp8_f32(o[4], o[5], w1, false); w1 = __builtin_amdgcn_cvt_pk_fp8_f32(o[6], o[7], w1, true);
;                     typedef unsigned u32x2_ __attribute__((ext_vector_type(2))); *(u32x2_*)((unsigned char*)O + off) = (u32x2_){w0, w1}; }
	v_mov_b32_e32 v129, v222
	v_pk_mul_f32 v[100:101], v[136:137], v[102:103]
	v_pk_mul_f32 v[94:95], v[130:131], v[94:95]
	v_cvt_f32_i32_e32 v92, v82
	v_pk_mul_f32 v[82:83], v[128:129], v[160:161]
	v_pk_mul_f32 v[86:87], v[122:123], v[86:87]
	v_mul_f32_e32 v101, v100, v101
	v_pk_mul_f32 v[90:91], v[134:135], v[90:91]
	v_mul_f32_e32 v84, v100, v83
	v_mul_f32_e32 v100, v86, v87
	v_mul_f32_e32 v87, v94, v83
	v_mul_f32_e32 v102, v90, v91
	v_exp_f32_e32 v87, v87
	v_mul_f32_e32 v90, v90, v83
	v_exp_f32_e32 v90, v90
	v_pk_mul_f32 v[96:97], v[132:133], v[96:97]
	v_add_f32_e32 v87, 1.0, v87
	v_mul_f32_e32 v95, v94, v95
	v_pk_mul_f32 v[92:93], v[114:115], v[92:93]
	v_rcp_f32_e32 v94, v87
	v_add_f32_e32 v87, 1.0, v90
	v_mul_f32_e32 v90, v96, v83
	v_exp_f32_e32 v90, v90
	v_mul_f32_e32 v91, v92, v83
	v_exp_f32_e32 v91, v91
	v_mul_f32_e32 v86, v86, v83
	v_mul_f32_e32 v93, v92, v93
	v_rcp_f32_e32 v92, v87
	v_add_f32_e32 v87, 1.0, v90
	v_exp_f32_e32 v86, v86
	v_exp_f32_e32 v84, v84
	v_rcp_f32_e32 v90, v87
	v_add_f32_e32 v87, 1.0, v91
	v_mul_f32_e32 v97, v96, v97
	v_rcp_f32_e32 v96, v87
	v_mul_f32_e32 v87, v82, v83
	v_exp_f32_e32 v87, v87
	v_add_f32_e32 v86, 1.0, v86
	v_add_f32_e32 v84, 1.0, v84
	v_rcp_f32_e32 v103, v86
	v_cvt_f32_i32_e32 v86, v88
	v_rcp_f32_e32 v84, v84
	v_add_f32_e32 v87, 1.0, v87
	v_rcp_f32_e32 v91, v87
	v_mov_b32_e32 v125, v222
	v_mov_b32_e32 v87, v222
	v_pk_mul_f32 v[86:87], v[124:125], v[86:87]
	v_cvt_f32_i32_e32 v88, v85
	v_mul_f32_e32 v84, v87, v84
	v_mul_f32_e32 v222, v101, v84
	v_mul_f32_e32 v84, v87, v94
	v_mul_f32_e32 v94, v95, v84
	v_mul_f32_e32 v84, v87, v92
	v_mul_f32_e32 v92, v102, v84
	v_mul_f32_e32 v84, v87, v90
	v_mul_f32_e32 v95, v97, v84
	v_mul_f32_e32 v84, v87, v96
	v_mul_f32_e32 v93, v93, v84
	v_pk_mul_f32 v[84:85], v[116:117], v[88:89]
	v_mov_b32_e32 v90, v82
	v_mul_f32_e32 v83, v84, v83
	v_exp_f32_e32 v83, v83
	v_mul_f32_e32 v88, v87, v103
	v_mul_f32_e32 v88, v100, v88
	v_mul_f32_e32 v88, 4.0, v88
	v_add_f32_e32 v82, 1.0, v83
	v_rcp_f32_e32 v89, v82
	v_pk_mul_f32 v[82:83], v[86:87], v[90:91]
	v_med3_f32 v88, v88, s62, v168
	v_mul_f32_e32 v82, v82, v83
	v_mul_f32_e32 v83, v84, v85
	v_mul_f32_e32 v84, v87, v89
	v_mul_f32_e32 v84, v83, v84
	v_mul_f32_e32 v83, 4.0, v222
	v_mul_f32_e32 v85, 4.0, v94
	v_mul_f32_e32 v82, 4.0, v82
	v_med3_f32 v83, v83, s62, v168
	v_med3_f32 v85, v85, s62, v168
	v_mul_f32_e32 v89, 4.0, v93
	v_med3_f32 v90, v82, s62, v168
	v_mov_b32_e32 v82, 0
	v_med3_f32 v89, v89, s62, v168
	v_cvt_pk_fp8_f32 v82, v83, v85
	v_mov_b32_e32 v83, 0
	v_cvt_pk_fp8_f32 v83, v89, v88
	v_mul_f32_e32 v86, 4.0, v92
	v_mul_f32_e32 v87, 4.0, v95
	v_mul_f32_e32 v84, 4.0, v84
	v_med3_f32 v86, v86, s62, v168
	v_med3_f32 v87, v87, s62, v168
	v_med3_f32 v84, v84, s62, v168
	v_cvt_pk_fp8_f32 v82, v86, v87 op_sel:[0,0,1]
	v_cvt_pk_fp8_f32 v83, v90, v84 op_sel:[0,0,1]
	v_cvt_f32_i32_e32 v87, v78
	v_cvt_f32_i32_e32 v86, v74
	v_cvt_f32_i32_e32 v78, v75
	v_cvt_f32_i32_e32 v75, v80
	v_cvt_f32_i32_e32 v80, v77
	v_cvt_f32_i32_e32 v77, v70
	v_cvt_f32_i32_e32 v160, v68
	v_cvt_f32_i32_e32 v70, v67
	v_or_b32_e32 v104, 32, v169
	v_cvt_f32_i32_e32 v74, v76
	v_mad_i64_i32 v[84:85], s[24:25], v104, s63, v[118:119]
	v_lshl_add_u64 v[84:85], v[84:85], 0, v[162:163]
	v_mov_b32_e32 v129, v223
	global_store_dwordx2 v[84:85], v[82:83], off
	v_pk_mul_f32 v[82:83], v[136:137], v[86:87]
	v_pk_mul_f32 v[78:79], v[130:131], v[78:79]
	v_cvt_f32_i32_e32 v76, v66
	v_pk_mul_f32 v[66:67], v[128:129], v[160:161]
	v_pk_mul_f32 v[70:71], v[122:123], v[70:71]
	v_mul_f32_e32 v83, v82, v83
	v_pk_mul_f32 v[74:75], v[134:135], v[74:75]
	v_mul_f32_e32 v68, v82, v67
	v_mul_f32_e32 v82, v70, v71
	v_mul_f32_e32 v71, v78, v67
	v_mul_f32_e32 v85, v74, v75
	v_exp_f32_e32 v71, v71
	v_mul_f32_e32 v74, v74, v67
	v_exp_f32_e32 v74, v74
	v_exp_f32_e32 v68, v68
	v_pk_mul_f32 v[80:81], v[132:133], v[80:81]
	v_add_f32_e32 v71, 1.0, v71
	v_mul_f32_e32 v79, v78, v79
	v_pk_mul_f32 v[76:77], v[114:115], v[76:77]
	v_rcp_f32_e32 v78, v71
	v_add_f32_e32 v71, 1.0, v74
	v_mul_f32_e32 v74, v80, v67
	v_exp_f32_e32 v74, v74
	v_mul_f32_e32 v75, v76, v67
	v_add_f32_e32 v68, 1.0, v68
	v_exp_f32_e32 v75, v75
	v_cvt_f32_i32_e32 v222, v72
	v_rcp_f32_e32 v68, v68
	v_mul_f32_e32 v77, v76, v77
	v_rcp_f32_e32 v76, v71
	v_add_f32_e32 v71, 1.0, v74
	v_mov_b32_e32 v125, v223
	v_mul_f32_e32 v81, v80, v81
	v_rcp_f32_e32 v80, v71
	v_add_f32_e32 v71, 1.0, v75
	v_pk_mul_f32 v[74:75], v[124:125], v[222:223]
	v_mul_f32_e32 v70, v70, v67
	v_rcp_f32_e32 v86, v71
	v_mul_f32_e32 v68, v75, v68
	v_exp_f32_e32 v70, v70
	v_mul_f32_e32 v83, v83, v68
	v_mul_f32_e32 v68, v75, v78
	v_cvt_f32_i32_e32 v72, v69
	v_mul_f32_e32 v78, v79, v68
	v_mul_f32_e32 v68, v75, v76
	v_mul_f32_e32 v76, v85, v68
	v_mul_f32_e32 v68, v75, v80
	v_mul_f32_e32 v79, v81, v68
	v_mul_f32_e32 v68, v75, v86
	v_mul_f32_e32 v71, v66, v67
	v_add_f32_e32 v70, 1.0, v70
	v_mul_f32_e32 v77, v77, v68
	v_pk_mul_f32 v[68:69], v[116:117], v[72:73]
	v_exp_f32_e32 v71, v71
	v_rcp_f32_e32 v70, v70
	v_mul_f32_e32 v67, v68, v67
	v_exp_f32_e32 v67, v67
	v_add_f32_e32 v71, 1.0, v71
	v_mul_f32_e32 v70, v75, v70
	v_rcp_f32_e32 v71, v71
	v_mul_f32_e32 v72, v82, v70
	v_mov_b32_e32 v70, v66
	v_add_f32_e32 v66, 1.0, v67
	v_rcp_f32_e32 v73, v66
	v_pk_mul_f32 v[66:67], v[74:75], v[70:71]
	v_mul_f32_e32 v72, 4.0, v72
	v_mul_f32_e32 v66, v66, v67
	v_mul_f32_e32 v67, v68, v69
	v_mul_f32_e32 v68, v75, v73
	v_mul_f32_e32 v68, v67, v68
	v_mul_f32_e32 v67, 4.0, v83
	v_mul_f32_e32 v69, 4.0, v78
	v_mul_f32_e32 v66, 4.0, v66
	v_med3_f32 v67, v67, s62, v168
	v_med3_f32 v69, v69, s62, v168
	v_mul_f32_e32 v73, 4.0, v77
	v_med3_f32 v74, v66, s62, v168
	v_mov_b32_e32 v66, 0
	v_med3_f32 v73, v73, s62, v168
	v_med3_f32 v72, v72, s62, v168
	v_cvt_pk_fp8_f32 v66, v67, v69
	v_mov_b32_e32 v67, 0
	v_cvt_pk_fp8_f32 v67, v73, v72
	v_mul_f32_e32 v70, 4.0, v76
	v_mul_f32_e32 v71, 4.0, v79
	v_mul_f32_e32 v68, 4.0, v68
	v_med3_f32 v70, v70, s62, v168
	v_med3_f32 v71, v71, s62, v168
	v_med3_f32 v68, v68, s62, v168
	v_cvt_pk_fp8_f32 v66, v70, v71 op_sel:[0,0,1]
	v_cvt_pk_fp8_f32 v67, v74, v68 op_sel:[0,0,1]
	v_or_b32_e32 v84, 48, v169
	v_mad_i64_i32 v[68:69], s[24:25], v84, s63, v[118:119]
	v_lshl_add_u64 v[68:69], v[68:69], 0, v[162:163]
	global_store_dwordx2 v[68:69], v[66:67], off
	s_nop 0
	v_cvt_f32_i32_e32 v71, v62
	v_cvt_f32_i32_e32 v70, v58
	v_cvt_f32_i32_e32 v62, v59
	v_cvt_f32_i32_e32 v59, v64
	v_cvt_f32_i32_e32 v64, v61
	v_cvt_f32_i32_e32 v61, v54
	v_cvt_f32_i32_e32 v160, v52
	v_cvt_f32_i32_e32 v54, v51
	v_cvt_f32_i32_e32 v58, v60
	s_waitcnt lgkmcnt(0)
; __device__ __forceinline__ float fast_sigmoid(float x) { return __builtin_amdgcn_rcpf(1.0f + __expf(-x)); }
;     __device__ __forceinline__ void operator()(const f32x4 (&acc)[2][2][4][2], const Unit& u, int wr, int wc, int fr, int fq) const {
;     ...
;             for (int m = 0; m < 4; ++m) { const size_t off = (size_t)(row0 + ai * HALF + m * 16) * ldc + col0;
;                 const float rs = IN8 ? rt.tab[sl * 256 + wr * 64 + ai * HALF + m * 16 + fr] : isc;
;                 const float rsn = rs * -1.4426950408889634f, rs2 = rs * rs; (void)rsn; (void)rs2;
;                 float o[8];
; #pragma unroll
;                 for (int n = 0; n < 2; ++n)
; #pragma unroll
;                     for (int e = 0; e < 4; ++e) { const float ga = acc[ai][0][m][n][e], ua = acc[ai][1][m][n][e];
;                         if (IN8) {
;                             const float gq = (float)__float_as_int(ga) * cg[n][e], uq = (float)__float_as_int(ua) * cu[n][e];
;                             const float sg = __builtin_amdgcn_rcpf(1.0f + __builtin_amdgcn_exp2f(gq * rsn));
;                             o[4 * n + e] = (gq * uq) * (sg * rs2); }
;                         else { const float g = ga * rs, up = ua * rs; o[4 * n + e] = g * fast_sigmoid(g) * up; } }
;                 if (F8) { unsigned w0 = 0u, w1 = 0u;
; #pragma unroll
;                     for (int e = 0; e < 8; ++e) o[e] = __builtin_amdgcn_fmed3f(o[e] * H8_SCALE, -448.0f, 448.0f);
;                     w0 = __builtin_amdgcn_cvt_pk_fp8_f32(o[0], o[1], w0, false); w0 = __builtin_amdgcn_cvt_pk_fp8_f32(o[2], o[3], w0, true);
;                     w1 = __builtin_amdgcn_cvt_pk_fp8_f32(o[4], o[5], w1, false); w1 = __builtin_amdgcn_cvt_pk_fp8_f32(o[6], o[7], w1, true);
;                     typedef unsigned u32x2_ __attribute__((ext_vector_type(2))); *(u32x2_*)((unsigned char*)O + off) = (u32x2_){w0, w1}; }
	v_mov_b32_e32 v129, v224
	v_pk_mul_f32 v[68:69], v[136:137], v[70:71]
	v_pk_mul_f32 v[62:63], v[130:131], v[62:63]
	v_cvt_f32_i32_e32 v60, v50
	v_pk_mul_f32 v[50:51], v[128:129], v[160:161]
	v_pk_mul_f32 v[54:55], v[122:123], v[54:55]
	v_mul_f32_e32 v69, v68, v69
	v_pk_mul_f32 v[58:59], v[134:135], v[58:59]
	v_mul_f32_e32 v52, v68, v51
	v_mul_f32_e32 v68, v54, v55
	v_mul_f32_e32 v55, v62, v51
	v_mul_f32_e32 v70, v58, v59
	v_exp_f32_e32 v55, v55
	v_mul_f32_e32 v58, v58, v51
	v_exp_f32_e32 v58, v58
	v_pk_mul_f32 v[64:65], v[132:133], v[64:65]
	v_add_f32_e32 v55, 1.0, v55
	v_mul_f32_e32 v63, v62, v63
	v_pk_mul_f32 v[60:61], v[114:115], v[60:61]
	v_rcp_f32_e32 v62, v55
	v_add_f32_e32 v55, 1.0, v58
	v_mul_f32_e32 v58, v64, v51
	v_exp_f32_e32 v58, v58
	v_mul_f32_e32 v59, v60, v51
	v_exp_f32_e32 v59, v59
	v_mul_f32_e32 v54, v54, v51
	v_mul_f32_e32 v61, v60, v61
	v_rcp_f32_e32 v60, v55
	v_add_f32_e32 v55, 1.0, v58
	v_exp_f32_e32 v54, v54
	v_exp_f32_e32 v52, v52
	v_rcp_f32_e32 v58, v55
	v_add_f32_e32 v55, 1.0, v59
	v_mul_f32_e32 v65, v64, v65
	v_rcp_f32_e32 v64, v55
	v_mul_f32_e32 v55, v50, v51
	v_exp_f32_e32 v55, v55
	v_add_f32_e32 v54, 1.0, v54
	v_add_f32_e32 v52, 1.0, v52
	v_rcp_f32_e32 v71, v54
	v_cvt_f32_i32_e32 v54, v56
	v_rcp_f32_e32 v52, v52
	v_add_f32_e32 v55, 1.0, v55
	v_rcp_f32_e32 v59, v55
	v_mov_b32_e32 v125, v224
	v_mov_b32_e32 v55, v224
	v_pk_mul_f32 v[54:55], v[124:125], v[54:55]
	v_cvt_f32_i32_e32 v56, v53
	v_mul_f32_e32 v52, v55, v52
	v_mul_f32_e32 v224, v69, v52
	v_mul_f32_e32 v52, v55, v62
	v_mul_f32_e32 v62, v63, v52
	v_mul_f32_e32 v52, v55, v60
	v_mul_f32_e32 v60, v70, v52
	v_mul_f32_e32 v52, v55, v58
	v_mul_f32_e32 v63, v65, v52
	v_mul_f32_e32 v52, v55, v64
	v_mul_f32_e32 v61, v61, v52
	v_pk_mul_f32 v[52:53], v[116:117], v[56:57]
	v_mov_b32_e32 v58, v50
	v_mul_f32_e32 v51, v52, v51
	v_exp_f32_e32 v51, v51
	v_mul_f32_e32 v56, v55, v71
	v_mul_f32_e32 v56, v68, v56
	v_mul_f32_e32 v56, 4.0, v56
	v_add_f32_e32 v50, 1.0, v51
	v_rcp_f32_e32 v57, v50
	v_pk_mul_f32 v[50:51], v[54:55], v[58:59]
	v_med3_f32 v56, v56, s62, v168
	v_mul_f32_e32 v50, v50, v51
	v_mul_f32_e32 v51, v52, v53
	v_mul_f32_e32 v52, v55, v57
	v_mul_f32_e32 v52, v51, v52
	v_mul_f32_e32 v51, 4.0, v224
	v_mul_f32_e32 v53, 4.0, v62
	v_mul_f32_e32 v50, 4.0, v50
	v_med3_f32 v51, v51, s62, v168
	v_med3_f32 v53, v53, s62, v168
	v_mul_f32_e32 v57, 4.0, v61
	v_med3_f32 v58, v50, s62, v168
	v_mov_b32_e32 v50, 0
	v_med3_f32 v57, v57, s62, v168
	v_cvt_pk_fp8_f32 v50, v51, v53
	v_mov_b32_e32 v51, 0
	v_cvt_pk_fp8_f32 v51, v57, v56
	v_mul_f32_e32 v54, 4.0, v60
	v_mul_f32_e32 v55, 4.0, v63
	v_mul_f32_e32 v52, 4.0, v52
	v_med3_f32 v54, v54, s62, v168
	v_med3_f32 v55, v55, s62, v168
	v_med3_f32 v52, v52, s62, v168
	v_cvt_pk_fp8_f32 v50, v54, v55 op_sel:[0,0,1]
	v_cvt_pk_fp8_f32 v51, v58, v52 op_sel:[0,0,1]
	v_cvt_f32_i32_e32 v55, v46
	v_cvt_f32_i32_e32 v54, v42
	v_cvt_f32_i32_e32 v46, v43
	v_cvt_f32_i32_e32 v43, v48
	v_cvt_f32_i32_e32 v48, v45
	v_cvt_f32_i32_e32 v45, v38
	v_cvt_f32_i32_e32 v160, v36
	v_cvt_f32_i32_e32 v38, v35
	v_add_u32_e32 v72, 0x80, v169
	v_cvt_f32_i32_e32 v42, v44
	v_mad_i64_i32 v[52:53], s[24:25], v72, s63, v[118:119]
	v_lshl_add_u64 v[52:53], v[52:53], 0, v[162:163]
	v_mov_b32_e32 v129, v225
	global_store_dwordx2 v[52:53], v[50:51], off
	v_pk_mul_f32 v[50:51], v[136:137], v[54:55]
	v_pk_mul_f32 v[46:47], v[130:131], v[46:47]
	v_cvt_f32_i32_e32 v44, v34
	v_pk_mul_f32 v[34:35], v[128:129], v[160:161]
	v_pk_mul_f32 v[38:39], v[122:123], v[38:39]
	v_mul_f32_e32 v51, v50, v51
	v_pk_mul_f32 v[42:43], v[134:135], v[42:43]
	v_mul_f32_e32 v36, v50, v35
	v_mul_f32_e32 v50, v38, v39
	v_mul_f32_e32 v39, v46, v35
	v_mul_f32_e32 v53, v42, v43
	v_exp_f32_e32 v39, v39
	v_mul_f32_e32 v42, v42, v35
	v_exp_f32_e32 v42, v42
	v_exp_f32_e32 v36, v36
	v_pk_mul_f32 v[48:49], v[132:133], v[48:49]
	v_add_f32_e32 v39, 1.0, v39
	v_mul_f32_e32 v47, v46, v47
	v_pk_mul_f32 v[44:45], v[114:115], v[44:45]
	v_rcp_f32_e32 v46, v39
	v_add_f32_e32 v39, 1.0, v42
	v_mul_f32_e32 v42, v48, v35
	v_exp_f32_e32 v42, v42
	v_mul_f32_e32 v43, v44, v35
	v_add_f32_e32 v36, 1.0, v36
	v_exp_f32_e32 v43, v43
	v_cvt_f32_i32_e32 v224, v40
	v_rcp_f32_e32 v36, v36
	v_mul_f32_e32 v45, v44, v45
	v_rcp_f32_e32 v44, v39
	v_add_f32_e32 v39, 1.0, v42
	v_mov_b32_e32 v125, v225
	v_mul_f32_e32 v49, v48, v49
	v_rcp_f32_e32 v48, v39
	v_add_f32_e32 v39, 1.0, v43
	v_pk_mul_f32 v[42:43], v[124:125], v[224:225]
	v_mul_f32_e32 v38, v38, v35
	v_rcp_f32_e32 v54, v39
	v_mul_f32_e32 v36, v43, v36
	v_exp_f32_e32 v38, v38
	v_mul_f32_e32 v51, v51, v36
	v_mul_f32_e32 v36, v43, v46
	v_cvt_f32_i32_e32 v40, v37
	v_mul_f32_e32 v46, v47, v36
	v_mul_f32_e32 v36, v43, v44
	v_mul_f32_e32 v44, v53, v36
	v_mul_f32_e32 v36, v43, v48
	v_mul_f32_e32 v47, v49, v36
	v_mul_f32_e32 v36, v43, v54
	v_mul_f32_e32 v39, v34, v35
	v_add_f32_e32 v38, 1.0, v38
	v_mul_f32_e32 v45, v45, v36
	v_pk_mul_f32 v[36:37], v[116:117], v[40:41]
	v_exp_f32_e32 v39, v39
	v_rcp_f32_e32 v38, v38
	v_mul_f32_e32 v35, v36, v35
	v_exp_f32_e32 v35, v35
	v_add_f32_e32 v39, 1.0, v39
	v_mul_f32_e32 v38, v43, v38
	v_rcp_f32_e32 v39, v39
	v_mul_f32_e32 v40, v50, v38
	v_mov_b32_e32 v38, v34
	v_add_f32_e32 v34, 1.0, v35
	v_rcp_f32_e32 v41, v34
	v_pk_mul_f32 v[34:35], v[42:43], v[38:39]
	v_mul_f32_e32 v40, 4.0, v40
	v_mul_f32_e32 v34, v34, v35
	v_mul_f32_e32 v35, v36, v37
	v_mul_f32_e32 v36, v43, v41
	v_mul_f32_e32 v36, v35, v36
	v_mul_f32_e32 v35, 4.0, v51
	v_mul_f32_e32 v37, 4.0, v46
	v_mul_f32_e32 v34, 4.0, v34
	v_med3_f32 v35, v35, s62, v168
	v_med3_f32 v37, v37, s62, v168
	v_mul_f32_e32 v41, 4.0, v45
	v_med3_f32 v42, v34, s62, v168
	v_mov_b32_e32 v34, 0
	v_med3_f32 v41, v41, s62, v168
	v_med3_f32 v40, v40, s62, v168
	v_cvt_pk_fp8_f32 v34, v35, v37
	v_mov_b32_e32 v35, 0
	v_cvt_pk_fp8_f32 v35, v41, v40
	v_mul_f32_e32 v38, 4.0, v44
	v_mul_f32_e32 v39, 4.0, v47
	v_mul_f32_e32 v36, 4.0, v36
	v_med3_f32 v38, v38, s62, v168
	v_med3_f32 v39, v39, s62, v168
	v_med3_f32 v36, v36, s62, v168
	v_cvt_pk_fp8_f32 v34, v38, v39 op_sel:[0,0,1]
	v_cvt_pk_fp8_f32 v35, v42, v36 op_sel:[0,0,1]
	v_add_u32_e32 v52, 0x90, v169
	v_mad_i64_i32 v[36:37], s[24:25], v52, s63, v[118:119]
	v_lshl_add_u64 v[36:37], v[36:37], 0, v[162:163]
	global_store_dwordx2 v[36:37], v[34:35], off
	s_nop 0
	v_cvt_f32_i32_e32 v39, v30
	v_cvt_f32_i32_e32 v38, v26
	v_cvt_f32_i32_e32 v30, v27
	v_cvt_f32_i32_e32 v27, v32
	v_cvt_f32_i32_e32 v32, v29
	v_cvt_f32_i32_e32 v29, v22
	v_cvt_f32_i32_e32 v160, v20
	v_cvt_f32_i32_e32 v22, v19
	v_cvt_f32_i32_e32 v26, v28
	s_waitcnt lgkmcnt(0)
; __device__ __forceinline__ float fast_sigmoid(float x) { return __builtin_amdgcn_rcpf(1.0f + __expf(-x)); }
;     __device__ __forceinline__ void operator()(const f32x4 (&acc)[2][2][4][2], const Unit& u, int wr, int wc, int fr, int fq) const {
;     ...
;             for (int m = 0; m < 4; ++m) { const size_t off = (size_t)(row0 + ai * HALF + m * 16) * ldc + col0;
;                 const float rs = IN8 ? rt.tab[sl * 256 + wr * 64 + ai * HALF + m * 16 + fr] : isc;
;                 const float rsn = rs * -1.4426950408889634f, rs2 = rs * rs; (void)rsn; (void)rs2;
;                 float o[8];
; #pragma unroll
;                 for (int n = 0; n < 2; ++n)
; #pragma unroll
;                     for (int e = 0; e < 4; ++e) { const float ga = acc[ai][0][m][n][e], ua = acc[ai][1][m][n][e];
;                         if (IN8) {
;                             const float gq = (float)__float_as_int(ga) * cg[n][e], uq = (float)__float_as_int(ua) * cu[n][e];
;                             const float sg = __builtin_amdgcn_rcpf(1.0f + __builtin_amdgcn_exp2f(gq * rsn));
;                             o[4 * n + e] = (gq * uq) * (sg * rs2); }
;                         else { const float g = ga * rs, up = ua * rs; o[4 * n + e] = g * fast_sigmoid(g) * up; } }
;                 if (F8) { unsigned w0 = 0u, w1 = 0u;
; #pragma unroll
;                     for (int e = 0; e < 8; ++e) o[e] = __builtin_amdgcn_fmed3f(o[e] * H8_SCALE, -448.0f, 448.0f);
;                     w0 = __builtin_amdgcn_cvt_pk_fp8_f32(o[0], o[1], w0, false); w0 = __builtin_amdgcn_cvt_pk_fp8_f32(o[2], o[3], w0, true);
;                     w1 = __builtin_amdgcn_cvt_pk_fp8_f32(o[4], o[5], w1, false); w1 = __builtin_amdgcn_cvt_pk_fp8_f32(o[6], o[7], w1, true);
;                     typedef unsigned u32x2_ __attribute__((ext_vector_type(2))); *(u32x2_*)((unsigned char*)O + off) = (u32x2_){w0, w1}; }
	v_mov_b32_e32 v129, v226
	v_pk_mul_f32 v[36:37], v[136:137], v[38:39]
	v_pk_mul_f32 v[30:31], v[130:131], v[30:31]
	v_cvt_f32_i32_e32 v28, v18
	v_pk_mul_f32 v[18:19], v[128:129], v[160:161]
	v_pk_mul_f32 v[22:23], v[122:123], v[22:23]
	v_mul_f32_e32 v37, v36, v37
	v_pk_mul_f32 v[26:27], v[134:135], v[26:27]
	v_mul_f32_e32 v20, v36, v19
	v_mul_f32_e32 v36, v22, v23
	v_mul_f32_e32 v23, v30, v19
	v_mul_f32_e32 v38, v26, v27
	v_exp_f32_e32 v23, v23
	v_mul_f32_e32 v26, v26, v19
	v_exp_f32_e32 v26, v26
	v_pk_mul_f32 v[32:33], v[132:133], v[32:33]
	v_add_f32_e32 v23, 1.0, v23
	v_mul_f32_e32 v31, v30, v31
	v_pk_mul_f32 v[28:29], v[114:115], v[28:29]
	v_rcp_f32_e32 v30, v23
	v_add_f32_e32 v23, 1.0, v26
	v_mul_f32_e32 v26, v32, v19
	v_exp_f32_e32 v26, v26
	v_mul_f32_e32 v27, v28, v19
	v_exp_f32_e32 v27, v27
	v_mul_f32_e32 v22, v22, v19
	v_mul_f32_e32 v29, v28, v29
	v_rcp_f32_e32 v28, v23
	v_add_f32_e32 v23, 1.0, v26
	v_exp_f32_e32 v22, v22
	v_exp_f32_e32 v20, v20
	v_rcp_f32_e32 v26, v23
	v_add_f32_e32 v23, 1.0, v27
	v_mul_f32_e32 v33, v32, v33
	v_rcp_f32_e32 v32, v23
	v_mul_f32_e32 v23, v18, v19
	v_exp_f32_e32 v23, v23
	v_add_f32_e32 v22, 1.0, v22
	v_add_f32_e32 v20, 1.0, v20
	v_rcp_f32_e32 v39, v22
	v_cvt_f32_i32_e32 v22, v24
	v_rcp_f32_e32 v20, v20
	v_add_f32_e32 v23, 1.0, v23
	v_rcp_f32_e32 v27, v23
	v_mov_b32_e32 v125, v226
	v_mov_b32_e32 v23, v226
	v_pk_mul_f32 v[22:23], v[124:125], v[22:23]
	v_cvt_f32_i32_e32 v24, v21
	v_mul_f32_e32 v20, v23, v20
	v_mul_f32_e32 v226, v37, v20
	v_mul_f32_e32 v20, v23, v30
	v_mul_f32_e32 v30, v31, v20
	v_mul_f32_e32 v20, v23, v28
	v_mul_f32_e32 v28, v38, v20
	v_mul_f32_e32 v20, v23, v26
	v_mul_f32_e32 v31, v33, v20
	v_mul_f32_e32 v20, v23, v32
	v_mul_f32_e32 v29, v29, v20
	v_pk_mul_f32 v[20:21], v[116:117], v[24:25]
	v_mov_b32_e32 v26, v18
	v_mul_f32_e32 v19, v20, v19
	v_exp_f32_e32 v19, v19
	v_mul_f32_e32 v24, v23, v39
	v_mul_f32_e32 v24, v36, v24
	v_mul_f32_e32 v24, 4.0, v24
	v_add_f32_e32 v18, 1.0, v19
	v_rcp_f32_e32 v25, v18
	v_pk_mul_f32 v[18:19], v[22:23], v[26:27]
	v_med3_f32 v24, v24, s62, v168
	v_mul_f32_e32 v18, v18, v19
	v_mul_f32_e32 v19, v20, v21
	v_mul_f32_e32 v20, v23, v25
	v_mul_f32_e32 v20, v19, v20
	v_mul_f32_e32 v19, 4.0, v226
	v_mul_f32_e32 v21, 4.0, v30
	v_mul_f32_e32 v18, 4.0, v18
	v_med3_f32 v19, v19, s62, v168
	v_med3_f32 v21, v21, s62, v168
	v_mul_f32_e32 v25, 4.0, v29
	v_med3_f32 v26, v18, s62, v168
	v_mov_b32_e32 v18, 0
	v_med3_f32 v25, v25, s62, v168
	v_cvt_pk_fp8_f32 v18, v19, v21
	v_mov_b32_e32 v19, 0
	v_cvt_pk_fp8_f32 v19, v25, v24
	v_mul_f32_e32 v22, 4.0, v28
	v_mul_f32_e32 v23, 4.0, v31
	v_mul_f32_e32 v20, 4.0, v20
	v_med3_f32 v22, v22, s62, v168
	v_med3_f32 v23, v23, s62, v168
	v_med3_f32 v20, v20, s62, v168
	v_cvt_pk_fp8_f32 v18, v22, v23 op_sel:[0,0,1]
	v_cvt_pk_fp8_f32 v19, v26, v20 op_sel:[0,0,1]
	v_cvt_f32_i32_e32 v23, v14
	v_cvt_f32_i32_e32 v22, v10
	v_cvt_f32_i32_e32 v14, v11
	v_cvt_f32_i32_e32 v11, v16
	v_cvt_f32_i32_e32 v16, v13
	v_cvt_f32_i32_e32 v13, v6
	v_cvt_f32_i32_e32 v160, v4
	v_cvt_f32_i32_e32 v6, v3
	v_add_u32_e32 v40, 0xa0, v169
	v_cvt_f32_i32_e32 v10, v12
	v_mad_i64_i32 v[20:21], s[24:25], v40, s63, v[118:119]
	v_lshl_add_u64 v[20:21], v[20:21], 0, v[162:163]
	v_mov_b32_e32 v129, v227
	global_store_dwordx2 v[20:21], v[18:19], off
	v_pk_mul_f32 v[18:19], v[136:137], v[22:23]
	v_pk_mul_f32 v[14:15], v[130:131], v[14:15]
	v_cvt_f32_i32_e32 v12, v2
	v_pk_mul_f32 v[2:3], v[128:129], v[160:161]
	v_pk_mul_f32 v[6:7], v[122:123], v[6:7]
	v_mul_f32_e32 v19, v18, v19
	v_pk_mul_f32 v[10:11], v[134:135], v[10:11]
	v_mul_f32_e32 v4, v18, v3
	v_mul_f32_e32 v18, v6, v7
	v_mul_f32_e32 v7, v14, v3
	v_mul_f32_e32 v21, v10, v11
	v_exp_f32_e32 v7, v7
	v_mul_f32_e32 v10, v10, v3
	v_exp_f32_e32 v10, v10
	v_exp_f32_e32 v4, v4
	v_pk_mul_f32 v[16:17], v[132:133], v[16:17]
	v_add_f32_e32 v7, 1.0, v7
	v_mul_f32_e32 v15, v14, v15
	v_pk_mul_f32 v[12:13], v[114:115], v[12:13]
	v_rcp_f32_e32 v14, v7
	v_add_f32_e32 v7, 1.0, v10
	v_mul_f32_e32 v10, v16, v3
	v_exp_f32_e32 v10, v10
	v_mul_f32_e32 v11, v12, v3
	v_add_f32_e32 v4, 1.0, v4
	v_exp_f32_e32 v11, v11
	v_cvt_f32_i32_e32 v226, v8
	v_rcp_f32_e32 v4, v4
	v_mul_f32_e32 v13, v12, v13
	v_rcp_f32_e32 v12, v7
	v_add_f32_e32 v7, 1.0, v10
	v_mov_b32_e32 v125, v227
	v_mul_f32_e32 v17, v16, v17
	v_rcp_f32_e32 v16, v7
	v_add_f32_e32 v7, 1.0, v11
	v_pk_mul_f32 v[10:11], v[124:125], v[226:227]
	v_mul_f32_e32 v6, v6, v3
	v_rcp_f32_e32 v22, v7
	v_mul_f32_e32 v4, v11, v4
	v_exp_f32_e32 v6, v6
	v_mul_f32_e32 v19, v19, v4
	v_mul_f32_e32 v4, v11, v14
	v_cvt_f32_i32_e32 v8, v5
	v_mul_f32_e32 v14, v15, v4
	v_mul_f32_e32 v4, v11, v12
	v_mul_f32_e32 v12, v21, v4
	v_mul_f32_e32 v4, v11, v16
	v_mul_f32_e32 v15, v17, v4
	v_mul_f32_e32 v4, v11, v22
	v_mul_f32_e32 v7, v2, v3
	v_add_f32_e32 v6, 1.0, v6
	v_mul_f32_e32 v13, v13, v4
	v_pk_mul_f32 v[4:5], v[116:117], v[8:9]
	v_exp_f32_e32 v7, v7
	v_rcp_f32_e32 v6, v6
	v_mul_f32_e32 v3, v4, v3
	v_exp_f32_e32 v3, v3
	v_add_f32_e32 v7, 1.0, v7
	v_mul_f32_e32 v6, v11, v6
	v_rcp_f32_e32 v7, v7
	v_mul_f32_e32 v8, v18, v6
	v_mov_b32_e32 v6, v2
	v_add_f32_e32 v2, 1.0, v3
	v_rcp_f32_e32 v9, v2
	v_pk_mul_f32 v[2:3], v[10:11], v[6:7]
	v_mul_f32_e32 v8, 4.0, v8
	v_mul_f32_e32 v2, v2, v3
	v_mul_f32_e32 v3, v4, v5
	v_mul_f32_e32 v4, v11, v9
	v_mul_f32_e32 v4, v3, v4
	v_mul_f32_e32 v3, 4.0, v19
	v_mul_f32_e32 v5, 4.0, v14
	v_mul_f32_e32 v2, 4.0, v2
	v_med3_f32 v3, v3, s62, v168
	v_med3_f32 v5, v5, s62, v168
	v_mul_f32_e32 v9, 4.0, v13
	v_med3_f32 v10, v2, s62, v168
	v_mov_b32_e32 v2, 0
	v_med3_f32 v9, v9, s62, v168
	v_med3_f32 v8, v8, s62, v168
	v_cvt_pk_fp8_f32 v2, v3, v5
	v_mov_b32_e32 v3, 0
	v_cvt_pk_fp8_f32 v3, v9, v8
	v_mul_f32_e32 v6, 4.0, v12
	v_mul_f32_e32 v7, 4.0, v15
	v_mul_f32_e32 v4, 4.0, v4
	v_med3_f32 v6, v6, s62, v168
	v_med3_f32 v7, v7, s62, v168
	v_med3_f32 v4, v4, s62, v168
	v_cvt_pk_fp8_f32 v2, v6, v7 op_sel:[0,0,1]
	v_cvt_pk_fp8_f32 v3, v10, v4 op_sel:[0,0,1]
	v_add_u32_e32 v20, 0xb0, v169
	v_mad_i64_i32 v[4:5], s[24:25], v20, s63, v[118:119]
	v_lshl_add_u64 v[4:5], v[4:5], 0, v[162:163]
	global_store_dwordx2 v[4:5], v[2:3], off
	s_cbranch_vccnz .LBB0_4136
	s_andn2_b64 vcc, exec, s[4:5]
	s_cbranch_vccnz .LBB0_4135
	s_barrier
	s_branch .LBB0_4135
